# retention output unit epilogue: the eight head-norm gain loads prefetched three ahead (were eight serialized load+vmcnt(0) round trips per unit), counted waits
# speedup vs baseline: 1.0014x; 1.0014x over previous
; #define LAS __attribute__((address_space(3)))
; __device__ __forceinline__ void lds_barrier() { asm volatile("s_waitcnt lgkmcnt(0)" ::: "memory"); __builtin_amdgcn_s_barrier(); asm volatile("" ::: "memory"); }
; __device__ __forceinline__ void retp_out_unit(int unit, const bf16_t* P, const float* rotg, const float* gamma_logit, const bf16_t* ST, const float* gain, bf16_t* AO, LAS unsigned char* lds) {
;     ...
;         const bf16x8 pa = __builtin_bit_cast(bf16x8, (u32x4){pk[0], pk[1], pk[2], pk[3]});
; #pragma unroll
;         for (int c = 0; c < 8; ++c) { const bf16x8 vf = tr_frag(lds + RP_V1 + (32 * m + 4 * q + trq) * R_RS + (16 * c + 4 * trp) * 2, 16 * R_RS);
;             acc[c] = __builtin_amdgcn_mfma_f32_16x16x32_bf16(vf, pa, acc[c], 0, 0, 0); }
;     }
; #pragma unroll
;     for (int d = 0; d < 2; ++d) {
;         if (d == 1) { lds_barrier();
; #pragma unroll
;             for (int i = 0; i < 4; ++i) { const int piece = tid + 512 * i, p = piece >> 4, ch = piece & 15;
;                 *(LAS u32x4*)(lds + RP_KS + p * R_RS + ch * 16) = sbr[i]; *(LAS u32x4*)(lds + RP_V1 + p * R_RS + ch * 16) = gtr[i]; }
;             lds_barrier(); }
;         const LAS unsigned char* sb = lds + (d ? RP_KS : RP_V2) + l15 * R_RS + (8 * q) * 2;
;         f32x4 t2[8];
; #pragma unroll
;         for (int c = 0; c < 8; ++c) t2[c] = (f32x4){0.f, 0.f, 0.f, 0.f};
; #pragma unroll
;         for (int kk = 0; kk < 4; ++kk)
; #pragma unroll
;             for (int c = 0; c < 8; ++c) { const bf16x8 sf = *(const LAS bf16x8*)(sb + (16 * c) * R_RS + 64 * kk); t2[c] = __builtin_amdgcn_mfma_f32_16x16x32_bf16(sf, qf[kk], t2[c], 0, 0, 0); }
.LBB0_403:
	v_mul_f32_e32 v78, v78, v98
	v_mul_f32_e32 v79, v79, v99
	v_mul_f32_e32 v80, v80, v100
	v_mul_f32_e32 v81, v81, v101
	v_cvt_pk_bf16_f32 v90, v78, v79
	v_mul_f32_e32 v78, v86, v104
	v_mul_f32_e32 v79, v87, v105
	v_mul_f32_e32 v86, v88, v102
	v_mul_f32_e32 v87, v89, v103
	v_cvt_pk_bf16_f32 v91, v80, v81
	v_cvt_pk_bf16_f32 v92, v78, v79
	ds_read_b64_tr_b16 v[80:81], v146 offset:32256
	ds_read_b64_tr_b16 v[78:79], v145 offset:64512
	v_cvt_pk_bf16_f32 v93, v86, v87
	ds_read_b64_tr_b16 v[88:89], v146 offset:32288
	ds_read_b64_tr_b16 v[86:87], v145 offset:64544
	ds_read_b64_tr_b16 v[94:95], v145 offset:64576
	ds_read_b64_tr_b16 v[98:99], v145 offset:64608
	ds_read_b64_tr_b16 v[96:97], v146 offset:32320
	ds_read_b64_tr_b16 v[100:101], v146 offset:32352
	s_waitcnt lgkmcnt(6)
	v_mfma_f32_16x16x32_bf16 v[50:53], v[78:81], v[90:93], v[50:53]
	v_ashrrev_i32_e32 v125, 31, v124
	v_readlane_b32 s2, v255, 3
	v_readlane_b32 s3, v255, 4
	s_waitcnt lgkmcnt(4)
	v_mfma_f32_16x16x32_bf16 v[54:57], v[86:89], v[90:93], v[54:57]
	ds_read_b64_tr_b16 v[86:87], v145 offset:64640
	ds_read_b64_tr_b16 v[88:89], v146 offset:32384
	s_add_i32 s57, s57, s85
	s_add_i32 s42, s42, s43
	s_waitcnt lgkmcnt(3)
	v_mfma_f32_16x16x32_bf16 v[58:61], v[94:97], v[90:93], v[58:61]
	s_sub_i32 s44, s44, s85
	s_waitcnt lgkmcnt(2)
	v_mfma_f32_16x16x32_bf16 v[78:81], v[98:101], v[90:93], v[82:85]
	s_nop 2
	ds_read_b64_tr_b16 v[84:85], v146 offset:32416
	ds_read_b64_tr_b16 v[82:83], v145 offset:64672
	ds_read_b64_tr_b16 v[94:95], v145 offset:64704
	ds_read_b64_tr_b16 v[98:99], v145 offset:64736
	ds_read_b64_tr_b16 v[96:97], v146 offset:32448
	ds_read_b64_tr_b16 v[100:101], v146 offset:32480
	s_waitcnt lgkmcnt(4)
	v_mfma_f32_16x16x32_bf16 v[70:73], v[82:85], v[90:93], v[70:73]
	ds_read_b128 v[82:85], v156
	v_mfma_f32_16x16x32_bf16 v[62:65], v[86:89], v[90:93], v[62:65]
	s_waitcnt lgkmcnt(2)
	v_mfma_f32_16x16x32_bf16 v[74:77], v[94:97], v[90:93], v[74:77]
	s_waitcnt lgkmcnt(1)
	v_mfma_f32_16x16x32_bf16 v[66:69], v[98:101], v[90:93], v[66:69]
	ds_read_b128 v[86:89], v179
	ds_read_b128 v[90:93], v157
	ds_read_b128 v[94:97], v178
	ds_read_b128 v[98:101], v177
	ds_read_b128 v[102:105], v176
	ds_read_b128 v[194:197], v175
	ds_read_b128 v[198:201], v174
	ds_read_b128 v[202:205], v173
	ds_read_b128 v[206:209], v172
	s_waitcnt lgkmcnt(9)
	v_mfma_f32_16x16x32_bf16 v[82:85], v[82:85], v[38:41], 0
	ds_read_b128 v[210:213], v166
	ds_read_b128 v[214:217], v167
	s_waitcnt lgkmcnt(10)
	v_mfma_f32_16x16x32_bf16 v[86:89], v[86:89], v[38:41], 0
	s_waitcnt lgkmcnt(1)
	v_mfma_f32_16x16x32_bf16 v[82:85], v[210:213], v[34:37], v[82:85]
	ds_read_b128 v[210:213], v171
	v_mfma_f32_16x16x32_bf16 v[86:89], v[206:209], v[34:37], v[86:89]
	ds_read_b128 v[206:209], v170
	v_mfma_f32_16x16x32_bf16 v[94:97], v[94:97], v[38:41], 0
	v_mfma_f32_16x16x32_bf16 v[98:101], v[98:101], v[38:41], 0
	s_waitcnt lgkmcnt(1)
	v_mfma_f32_16x16x32_bf16 v[94:97], v[210:213], v[34:37], v[94:97]
	ds_read_b128 v[210:213], v169
	s_waitcnt lgkmcnt(1)
	v_mfma_f32_16x16x32_bf16 v[98:101], v[206:209], v[34:37], v[98:101]
	ds_read_b128 v[206:209], v168
	v_mfma_f32_16x16x32_bf16 v[102:105], v[102:105], v[38:41], 0
	v_mfma_f32_16x16x32_bf16 v[194:197], v[194:197], v[38:41], 0
	v_mfma_f32_16x16x32_bf16 v[198:201], v[198:201], v[38:41], 0
	v_mfma_f32_16x16x32_bf16 v[202:205], v[202:205], v[38:41], 0
	s_waitcnt lgkmcnt(1)
	v_mfma_f32_16x16x32_bf16 v[102:105], v[210:213], v[34:37], v[102:105]
	s_waitcnt lgkmcnt(0)
	v_mfma_f32_16x16x32_bf16 v[194:197], v[206:209], v[34:37], v[194:197]
	ds_read_b128 v[206:209], v165
	ds_read_b128 v[210:213], v164
	v_mfma_f32_16x16x32_bf16 v[198:201], v[214:217], v[34:37], v[198:201]
	s_waitcnt lgkmcnt(1)
	v_mfma_f32_16x16x32_bf16 v[202:205], v[206:209], v[34:37], v[202:205]
	ds_read_b128 v[206:209], v158
	ds_read_b128 v[214:217], v159
	s_waitcnt lgkmcnt(1)
	v_mfma_f32_16x16x32_bf16 v[82:85], v[206:209], v[46:49], v[82:85]
	ds_read_b128 v[206:209], v163
	v_mfma_f32_16x16x32_bf16 v[86:89], v[210:213], v[46:49], v[86:89]
	ds_read_b128 v[210:213], v162
	s_waitcnt lgkmcnt(1)
	v_mfma_f32_16x16x32_bf16 v[94:97], v[206:209], v[46:49], v[94:97]
	ds_read_b128 v[206:209], v161
	s_waitcnt lgkmcnt(1)
	v_mfma_f32_16x16x32_bf16 v[98:101], v[210:213], v[46:49], v[98:101]
	ds_read_b128 v[210:213], v160
	s_waitcnt lgkmcnt(1)
	v_mfma_f32_16x16x32_bf16 v[102:105], v[206:209], v[46:49], v[102:105]
	ds_read_b128 v[206:209], v149
	s_waitcnt lgkmcnt(1)
	v_mfma_f32_16x16x32_bf16 v[194:197], v[210:213], v[46:49], v[194:197]
	v_mfma_f32_16x16x32_bf16 v[90:93], v[90:93], v[46:49], v[202:205]
	s_nop 2
	ds_read_b128 v[202:205], v155
	ds_read_b128 v[210:213], v148
	s_waitcnt lgkmcnt(2)
	v_mfma_f32_16x16x32_bf16 v[82:85], v[206:209], v[42:45], v[82:85]
	ds_read_b128 v[206:209], v154
	v_mfma_f32_16x16x32_bf16 v[198:201], v[214:217], v[46:49], v[198:201]
	s_waitcnt lgkmcnt(2)
	v_mfma_f32_16x16x32_bf16 v[86:89], v[202:205], v[42:45], v[86:89]
	ds_read_b128 v[202:205], v153
	ds_read_b128 v[214:217], v152
	s_waitcnt lgkmcnt(2)
	v_mfma_f32_16x16x32_bf16 v[94:97], v[206:209], v[42:45], v[94:97]
	ds_read_b128 v[206:209], v150
	ds_read_b128 v[218:221], v151
	s_waitcnt lgkmcnt(0)
	s_barrier
	ds_write_b128 v107, v[6:9]
	ds_write_b128 v107, v[2:5] offset:36864
	ds_write_b128 v108, v[14:17]
	ds_write_b128 v108, v[10:13] offset:36864
	ds_write_b128 v109, v[22:25]
	ds_write_b128 v109, v[18:21] offset:36864
	ds_write_b128 v119, v[30:33]
	ds_write_b128 v119, v[26:29] offset:36864
	s_waitcnt lgkmcnt(0)
	s_barrier
; #define LAS __attribute__((address_space(3)))
; __device__ __forceinline__ void retp_out_unit(int unit, const bf16_t* P, const float* rotg, const float* gamma_logit, const bf16_t* ST, const float* gain, bf16_t* AO, LAS unsigned char* lds) {
;     ...
;         const LAS unsigned char* sb = lds + (d ? RP_KS : RP_V2) + l15 * R_RS + (8 * q) * 2;
;         f32x4 t2[8];
; #pragma unroll
;         for (int c = 0; c < 8; ++c) t2[c] = (f32x4){0.f, 0.f, 0.f, 0.f};
; #pragma unroll
;         for (int kk = 0; kk < 4; ++kk)
; #pragma unroll
;             for (int c = 0; c < 8; ++c) { const bf16x8 sf = *(const LAS bf16x8*)(sb + (16 * c) * R_RS + 64 * kk); t2[c] = __builtin_amdgcn_mfma_f32_16x16x32_bf16(sf, qf[kk], t2[c], 0, 0, 0); }
;         const float sc = d ? exp2f(lgb * (float)(128 - tl)) : exp2f(lgf * (float)(tl + 1));
; #pragma unroll
;         for (int c = 0; c < 8; ++c) acc[c] += t2[c] * sc;
;     }
	ds_read_b128 v[18:21], v147
	ds_read_b128 v[22:25], v147 offset:64
	ds_read_b128 v[26:29], v147 offset:4608
	ds_read_b128 v[30:33], v147 offset:4672
	s_waitcnt lgkmcnt(14)
	v_mfma_f32_16x16x32_bf16 v[2:5], v[214:217], v[42:45], v[102:105]
	v_add_u32_e32 v107, 1, v106
	v_cvt_f32_u32_e32 v107, v107
	v_mfma_f32_16x16x32_bf16 v[14:17], v[210:213], v[42:45], v[90:93]
	s_nop 2
	ds_read_b128 v[90:93], v147 offset:9216
	ds_read_b128 v[102:105], v147 offset:9280
	s_waitcnt lgkmcnt(5)
	v_mfma_f32_16x16x32_bf16 v[18:21], v[18:21], v[38:41], 0
	s_waitcnt lgkmcnt(3)
	v_mfma_f32_16x16x32_bf16 v[26:29], v[26:29], v[38:41], 0
	s_waitcnt lgkmcnt(1)
	v_mfma_f32_16x16x32_bf16 v[90:93], v[90:93], v[38:41], 0
	v_mfma_f32_16x16x32_bf16 v[18:21], v[22:25], v[34:37], v[18:21]
	v_mfma_f32_16x16x32_bf16 v[22:25], v[30:33], v[34:37], v[26:29]
	v_mul_f32_e32 v30, v123, v107
	v_cmp_gt_f32_e32 vcc, s56, v30
	v_mfma_f32_16x16x32_bf16 v[6:9], v[218:221], v[42:45], v[194:197]
	v_mfma_f32_16x16x32_bf16 v[10:13], v[206:209], v[42:45], v[198:201]
	s_nop 1
	ds_read_b128 v[194:197], v147 offset:13824
	ds_read_b128 v[198:201], v147 offset:13888
	s_waitcnt lgkmcnt(2)
	v_mfma_f32_16x16x32_bf16 v[26:29], v[102:105], v[34:37], v[90:93]
	v_cndmask_b32_e32 v103, 0, v190, vcc
	s_nop 1
	v_cndmask_b32_e32 v90, 0, v189, vcc
	v_fmac_f32_e32 v90, v123, v107
	v_mfma_f32_16x16x32_bf16 v[98:101], v[202:205], v[42:45], v[98:101]
	ds_read_b128 v[202:205], v147 offset:18432
	ds_read_b128 v[206:209], v147 offset:18496
	v_exp_f32_e32 v102, v90
	ds_read_b128 v[210:213], v147 offset:23040
	ds_read_b128 v[214:217], v147 offset:23104
	s_waitcnt lgkmcnt(5)
	v_mfma_f32_16x16x32_bf16 v[194:197], v[194:197], v[38:41], 0
	ds_read_b128 v[218:221], v147 offset:27648
	ds_read_b128 v[222:225], v147 offset:27712
	v_ldexp_f32 v108, v102, v103
	ds_read_b128 v[230:233], v147 offset:32256
	ds_read_b128 v[234:237], v147 offset:32320
	s_waitcnt lgkmcnt(7)
	v_mfma_f32_16x16x32_bf16 v[202:205], v[202:205], v[38:41], 0
	v_fma_f32 v60, v108, v96, v60
	v_fma_f32 v61, v108, v97, v61
	v_pk_fma_f32 v[94:95], v[108:109], v[94:95], v[58:59] op_sel_hi:[0,1,1]
	v_mov_b32_e32 v123, v111
	v_mfma_f32_16x16x32_bf16 v[30:33], v[198:201], v[34:37], v[194:197]
	v_fma_f32 v198, v108, v12, v76
	v_fma_f32 v199, v108, v13, v77
	v_pk_fma_f32 v[200:201], v[108:109], v[10:11], v[74:75] op_sel_hi:[0,1,1]
	v_pk_fma_f32 v[196:197], v[108:109], v[14:15], v[66:67] op_sel_hi:[0,1,1]
	ds_read_b128 v[12:15], v147 offset:128
	s_waitcnt lgkmcnt(7)
	v_mfma_f32_16x16x32_bf16 v[90:93], v[206:209], v[34:37], v[202:205]
	v_fma_f32 v194, v108, v16, v68
	v_fma_f32 v195, v108, v17, v69
	v_pk_fma_f32 v[206:207], v[108:109], v[4:5], v[64:65] op_sel_hi:[0,1,1]
	v_pk_fma_f32 v[208:209], v[108:109], v[2:3], v[62:63] op_sel_hi:[0,1,1]
	v_pk_fma_f32 v[202:203], v[108:109], v[8:9], v[72:73] op_sel_hi:[0,1,1]
	ds_read_b128 v[8:11], v147 offset:4736
	s_waitcnt lgkmcnt(7)
	v_mfma_f32_16x16x32_bf16 v[210:213], v[210:213], v[38:41], 0
	v_fma_f32 v204, v108, v6, v70
	v_fma_f32 v205, v108, v7, v71
	s_waitcnt lgkmcnt(5)
	v_mfma_f32_16x16x32_bf16 v[218:221], v[218:221], v[38:41], 0
	s_waitcnt lgkmcnt(3)
	v_mfma_f32_16x16x32_bf16 v[38:41], v[230:233], v[38:41], 0
	v_mfma_f32_16x16x32_bf16 v[102:105], v[214:217], v[34:37], v[210:213]
	v_mfma_f32_16x16x32_bf16 v[66:69], v[222:225], v[34:37], v[218:221]
	s_nop 1
	v_fma_f32 v210, v108, v100, v80
	v_fma_f32 v211, v108, v101, v81
	v_pk_fma_f32 v[212:213], v[108:109], v[98:99], v[78:79] op_sel_hi:[0,1,1]
	s_waitcnt lgkmcnt(2)
	v_mfma_f32_16x16x32_bf16 v[34:37], v[234:237], v[34:37], v[38:41]
	s_nop 2
	ds_read_b128 v[38:41], v147 offset:9344
	ds_read_b128 v[70:73], v147 offset:192
	s_waitcnt lgkmcnt(3)
	v_mfma_f32_16x16x32_bf16 v[12:15], v[12:15], v[46:49], v[18:21]
	ds_read_b128 v[4:7], v147 offset:13952
	s_nop 1
	ds_read_b128 v[16:19], v147 offset:4800
	s_waitcnt lgkmcnt(4)
	v_mfma_f32_16x16x32_bf16 v[8:11], v[8:11], v[46:49], v[22:25]
	s_nop 2
	ds_read_b128 v[20:23], v147 offset:18560
	ds_read_b128 v[62:65], v147 offset:9408
	s_waitcnt lgkmcnt(3)
	v_mfma_f32_16x16x32_bf16 v[2:5], v[4:7], v[46:49], v[30:33]
	v_sub_u32_e32 v6, 0x80, v106
	v_cvt_f32_i32_e32 v6, v6
	v_mul_f32_e32 v7, v121, v6
	v_mfma_f32_16x16x32_bf16 v[24:27], v[38:41], v[46:49], v[26:29]
	ds_read_b128 v[38:41], v147 offset:23168
	ds_read_b128 v[74:77], v147 offset:14016
	s_nop 0
	ds_read_b128 v[28:31], v147 offset:27776
	ds_read_b128 v[78:81], v147 offset:18624
	v_cmp_gt_f32_e32 vcc, s56, v7
	s_waitcnt lgkmcnt(5)
	v_mfma_f32_16x16x32_bf16 v[20:23], v[20:23], v[46:49], v[90:93]
	s_nop 2
	ds_read_b128 v[90:93], v147 offset:32384
	ds_read_b128 v[96:99], v147 offset:23232
	v_pk_fma_f32 v[32:33], v[108:109], v[88:89], v[56:57] op_sel_hi:[0,1,1]
	ds_read_b128 v[56:59], v147 offset:27840
	s_waitcnt lgkmcnt(6)
	v_mfma_f32_16x16x32_bf16 v[38:41], v[38:41], v[46:49], v[102:105]
	s_waitcnt lgkmcnt(4)
	v_mfma_f32_16x16x32_bf16 v[66:69], v[28:31], v[46:49], v[66:69]
	s_nop 0
	ds_read_b128 v[100:103], v147 offset:32448
	v_pk_fma_f32 v[28:29], v[108:109], v[86:87], v[54:55] op_sel_hi:[0,1,1]
	v_pk_fma_f32 v[30:31], v[108:109], v[84:85], v[52:53] op_sel_hi:[0,1,1]
	s_waitcnt lgkmcnt(3)
	v_mfma_f32_16x16x32_bf16 v[46:49], v[90:93], v[46:49], v[34:37]
	s_nop 2
	v_cndmask_b32_e32 v34, 0, v189, vcc
	v_fmac_f32_e32 v34, v121, v6
	v_exp_f32_e32 v34, v34
	v_mfma_f32_16x16x32_bf16 v[6:9], v[16:19], v[42:45], v[8:11]
	v_cndmask_b32_e32 v35, 0, v190, vcc
	v_mfma_f32_16x16x32_bf16 v[2:5], v[74:77], v[42:45], v[2:5]
	s_nop 0
	v_fma_f32 v10, v108, v82, v50
	v_fma_f32 v11, v108, v83, v51
	v_ldexp_f32 v50, v34, v35
	s_nop 1
	v_pk_fma_f32 v[32:33], v[50:51], v[8:9], v[32:33] op_sel_hi:[0,1,1]
	v_mfma_f32_16x16x32_bf16 v[12:15], v[70:73], v[42:45], v[12:15]
	v_fma_f32 v34, v50, v6, v28
	v_fma_f32 v35, v50, v7, v29
	v_mfma_f32_16x16x32_bf16 v[16:19], v[62:65], v[42:45], v[24:27]
	v_mfma_f32_16x16x32_bf16 v[6:9], v[78:81], v[42:45], v[20:23]
	s_nop 1
	v_fma_f32 v24, v50, v4, v210
	v_fma_f32 v25, v50, v5, v211
	v_pk_fma_f32 v[26:27], v[50:51], v[2:3], v[212:213] op_sel_hi:[0,1,1]
	v_pk_fma_f32 v[36:37], v[50:51], v[14:15], v[30:31] op_sel_hi:[0,1,1]
	s_waitcnt lgkmcnt(2)
; #define LAS __attribute__((address_space(3)))
; __device__ __forceinline__ void retp_out_unit(int unit, const bf16_t* P, const float* rotg, const float* gamma_logit, const bf16_t* ST, const float* gain, bf16_t* AO, LAS unsigned char* lds) {
;     ...
;     float ss = 0.f;
; #pragma unroll
;     for (int c = 0; c < 8; ++c) ss += (acc[c][0] * acc[c][0] + acc[c][1] * acc[c][1]) + (acc[c][2] * acc[c][2] + acc[c][3] * acc[c][3]);
;     ss += __shfl_xor(ss, 16); ss += __shfl_xor(ss, 32);
;     const float rstd = rsqrtf(ss * (1.f / 128.f) + EPS);
;     const LAS unsigned char* gp = lds + RP_V1 + tl * R_RS + (4 * q) * 2; bf16_t* op = AO + (size_t)row * D + h * 128 + 4 * q; const float* gn = gain + h * 128 + 4 * q;
; #pragma unroll
;     for (int c = 0; c < 8; ++c) { const u32x2 gw = *(const LAS u32x2*)(gp + 32 * c); const f32x4 g4 = *(const f32x4*)(gn + 16 * c);
	v_mfma_f32_16x16x32_bf16 v[2:5], v[96:99], v[42:45], v[38:41]
	v_fma_f32 v52, v50, v12, v10
	v_fma_f32 v53, v50, v13, v11
	v_pk_fma_f32 v[30:31], v[50:51], v[16:17], v[94:95] op_sel_hi:[0,1,1]
	v_pk_fma_f32 v[22:23], v[50:51], v[6:7], v[208:209] op_sel_hi:[0,1,1]
	s_waitcnt lgkmcnt(0)
	v_mfma_f32_16x16x32_bf16 v[12:15], v[100:103], v[42:45], v[46:49]
	v_fma_f32 v28, v50, v18, v60
	v_fma_f32 v29, v50, v19, v61
	v_pk_fma_f32 v[16:17], v[50:51], v[4:5], v[202:203] op_sel_hi:[0,1,1]
	v_pk_fma_f32 v[20:21], v[50:51], v[8:9], v[206:207] op_sel_hi:[0,1,1]
	v_mfma_f32_16x16x32_bf16 v[4:7], v[56:59], v[42:45], v[66:69]
	v_fma_f32 v18, v50, v2, v204
	v_fma_f32 v19, v50, v3, v205
	s_nop 0
	v_pk_fma_f32 v[2:3], v[50:51], v[14:15], v[194:195] op_sel_hi:[0,1,1]
	v_mov_b32_e32 v8, v52
	v_mov_b32_e32 v9, v34
	v_mov_b32_e32 v14, v37
	s_nop 0
	v_pk_fma_f32 v[10:11], v[50:51], v[4:5], v[200:201] op_sel_hi:[0,1,1]
	v_pk_fma_f32 v[4:5], v[50:51], v[12:13], v[196:197] op_sel_hi:[0,1,1]
	v_mov_b32_e32 v12, v53
	v_mov_b32_e32 v13, v35
	v_pk_mul_f32 v[12:13], v[12:13], v[12:13]
	v_mov_b32_e32 v15, v33
	v_pk_fma_f32 v[8:9], v[8:9], v[8:9], v[12:13]
	v_mov_b32_e32 v12, v36
	v_mov_b32_e32 v13, v32
	v_pk_mul_f32 v[14:15], v[14:15], v[14:15]
	v_mul_f32_e32 v42, v23, v23
	v_pk_fma_f32 v[12:13], v[12:13], v[12:13], v[14:15]
	v_pk_mul_f32 v[14:15], v[30:31], v[30:31]
	v_pk_add_f32 v[8:9], v[8:9], v[12:13]
	v_pk_mul_f32 v[12:13], v[28:29], v[28:29]
	v_pk_add_f32 v[8:9], v[8:9], v[8:9] op_sel:[0,1] op_sel_hi:[1,0]
	v_pk_mov_b32 v[38:39], v[14:15], v[12:13] op_sel:[1,0]
	v_mov_b32_e32 v15, v13
	v_pk_add_f32 v[12:13], v[38:39], v[14:15]
	v_mul_f32_e32 v14, v22, v22
	v_mov_b32_e32 v9, v14
	v_pk_add_f32 v[14:15], v[12:13], v[12:13] op_sel:[0,1] op_sel_hi:[1,0]
	v_lshlrev_b64 v[12:13], 12, v[124:125]
	v_lshl_add_u64 v[12:13], s[2:3], 0, v[12:13]
	v_lshl_add_u64 v[46:47], v[12:13], 0, s[36:37]
	s_lshl_b32 s36, s58, 2
	v_lshl_add_u64 v[12:13], v[116:117], 0, s[36:37]
	global_load_dwordx4 v[38:41], v[12:13], off
	global_load_dwordx4 v[240:243], v[12:13], off offset:64
	global_load_dwordx4 v[244:247], v[12:13], off offset:128
	global_load_dwordx4 v[248:251], v[12:13], off offset:192
	v_mov_b32_e32 v15, v42
	v_pk_add_f32 v[8:9], v[8:9], v[14:15]
	v_mul_f32_e32 v14, v27, v27
	v_mul_f32_e32 v43, v20, v20
	v_pk_fma_f32 v[14:15], v[26:27], v[26:27], v[14:15] op_sel_hi:[1,1,0]
	v_mul_f32_e32 v42, v25, v25
	v_mul_f32_e32 v44, v21, v21
	v_mov_b32_e32 v15, v43
	v_pk_fma_f32 v[42:43], v[24:25], v[24:25], v[42:43] op_sel_hi:[1,1,0]
	v_pk_fma_f32 v[6:7], v[50:51], v[6:7], v[198:199] op_sel_hi:[0,1,1]
	v_mov_b32_e32 v43, v44
	v_pk_add_f32 v[14:15], v[14:15], v[42:43]
	v_pk_mul_f32 v[42:43], v[18:19], v[18:19]
	v_pk_add_f32 v[8:9], v[8:9], v[14:15]
	v_pk_mul_f32 v[14:15], v[16:17], v[16:17]
	v_pk_add_f32 v[8:9], v[8:9], v[8:9] op_sel:[0,1] op_sel_hi:[1,0]
	v_pk_mov_b32 v[44:45], v[42:43], v[14:15] op_sel:[1,0]
	v_mov_b32_e32 v43, v15
	v_pk_add_f32 v[14:15], v[44:45], v[42:43]
	v_mul_f32_e32 v42, v4, v4
	v_mul_f32_e32 v43, v5, v5
	v_pk_add_f32 v[14:15], v[14:15], v[14:15] op_sel:[0,1] op_sel_hi:[1,0]
	v_mov_b32_e32 v9, v42
	v_mov_b32_e32 v15, v43
	v_pk_add_f32 v[8:9], v[8:9], v[14:15]
	v_mul_f32_e32 v14, v11, v11
	v_mul_f32_e32 v42, v7, v7
	v_mul_f32_e32 v44, v2, v2
	v_mul_f32_e32 v45, v3, v3
	v_pk_fma_f32 v[14:15], v[10:11], v[10:11], v[14:15] op_sel_hi:[1,1,0]
	v_pk_fma_f32 v[42:43], v[6:7], v[6:7], v[42:43] op_sel_hi:[1,1,0]
	v_mov_b32_e32 v15, v44
	v_mov_b32_e32 v43, v45
	v_pk_add_f32 v[14:15], v[14:15], v[42:43]
	s_cmpk_lt_i32 s57, 0x440
	v_pk_add_f32 v[8:9], v[8:9], v[14:15]
	v_and_b32_e32 v14, 64, v192
	v_add_f32_e32 v8, v8, v9
	v_xor_b32_e32 v9, 16, v192
	v_add_u32_e32 v14, 64, v14
	v_cmp_lt_i32_e32 vcc, v9, v14
	s_nop 1
	v_cndmask_b32_e32 v9, v192, v9, vcc
	v_lshlrev_b32_e32 v9, 2, v9
	ds_bpermute_b32 v9, v9, v8
	s_waitcnt lgkmcnt(0)
	v_add_f32_e32 v8, v8, v9
	v_xor_b32_e32 v9, 32, v192
	v_cmp_lt_i32_e32 vcc, v9, v14
	s_nop 1
	v_cndmask_b32_e32 v9, v192, v9, vcc
	v_lshlrev_b32_e32 v9, 2, v9
	ds_bpermute_b32 v9, v9, v8
	s_waitcnt lgkmcnt(0)
	v_add_f32_e32 v8, v8, v9
	v_fmamk_f32 v14, v8, 0x3c000000, v187
	v_mad_u64_u32 v[8:9], s[2:3], v106, s41, v[114:115]
	v_add_u32_e32 v15, 0x9000, v8
	ds_read2_b64 v[42:45], v15 offset1:4
	s_mov_b32 s2, 0x800000
	v_mul_f32_e32 v8, 0x4b800000, v14
	v_cmp_gt_f32_e32 vcc, s2, v14
	s_waitcnt lgkmcnt(0)
	v_lshlrev_b32_e32 v50, 16, v42
	v_cndmask_b32_e32 v8, v14, v8, vcc
	v_and_b32_e32 v42, 0xffff0000, v42
	v_rsq_f32_e32 v14, v8
	v_mul_f32_e32 v8, 0xbfb8aa3b, v50
	v_mul_f32_e32 v9, 0xbfb8aa3b, v42
	v_exp_f32_e32 v8, v8
	v_exp_f32_e32 v9, v9
	v_mul_f32_e32 v48, 0x45800000, v14
	v_cndmask_b32_e32 v14, v14, v48, vcc
	v_pk_mul_f32 v[36:37], v[36:37], v[14:15] op_sel_hi:[1,0]
	v_pk_add_f32 v[48:49], v[8:9], 1.0 op_sel_hi:[1,0]
	v_lshl_add_u64 v[8:9], v[46:47], 0, v[122:123]
	v_div_scale_f32 v51, s[2:3], v49, v49, v42
	v_rcp_f32_e32 v54, v51
	v_pk_mul_f32 v[46:47], v[52:53], v[14:15] op_sel_hi:[1,0]
	v_and_b32_e32 v53, 0xffff0000, v43
	s_waitcnt vmcnt(3)
; #define LAS __attribute__((address_space(3)))
; __device__ __forceinline__ float bflo(unsigned w) { return __uint_as_float(w << 16); }
; __device__ __forceinline__ float bfhi(unsigned w) { return __uint_as_float(w & 0xffff0000u); }
; __device__ __forceinline__ float silu_f(float x) { return x / (1.f + __expf(-x)); }
; __device__ __forceinline__ void retp_out_unit(int unit, const bf16_t* P, const float* rotg, const float* gamma_logit, const bf16_t* ST, const float* gain, bf16_t* AO, LAS unsigned char* lds) {
;     ...
;     const LAS unsigned char* gp = lds + RP_V1 + tl * R_RS + (4 * q) * 2; bf16_t* op = AO + (size_t)row * D + h * 128 + 4 * q; const float* gn = gain + h * 128 + 4 * q;
; #pragma unroll
;     for (int c = 0; c < 8; ++c) { const u32x2 gw = *(const LAS u32x2*)(gp + 32 * c); const f32x4 g4 = *(const f32x4*)(gn + 16 * c);
;         u32x2 o; o.x = pk2(acc[c][0] * rstd * g4[0] * silu_f(bflo(gw.x)), acc[c][1] * rstd * g4[1] * silu_f(bfhi(gw.x)));
;         o.y = pk2(acc[c][2] * rstd * g4[2] * silu_f(bflo(gw.y)), acc[c][3] * rstd * g4[3] * silu_f(bfhi(gw.y)));
;         *(u32x2*)(op + 16 * c) = o; }
	v_pk_mul_f32 v[38:39], v[38:39], v[46:47]
	v_fma_f32 v46, -v51, v54, 1.0
	v_fmac_f32_e32 v54, v46, v54
	v_div_scale_f32 v46, vcc, v42, v49, v42
	v_mul_f32_e32 v47, v46, v54
	v_fma_f32 v52, -v51, v47, v46
	v_fmac_f32_e32 v47, v52, v54
	v_fma_f32 v46, -v51, v47, v46
	v_div_scale_f32 v51, s[2:3], v48, v48, v50
	v_rcp_f32_e32 v52, v51
	v_div_fmas_f32 v46, v46, v54, v47
	v_div_fixup_f32 v47, v46, v49, v42
	v_pk_mul_f32 v[36:37], v[40:41], v[36:37]
	v_fma_f32 v42, -v51, v52, 1.0
	v_fmac_f32_e32 v52, v42, v52
	v_div_scale_f32 v42, vcc, v50, v48, v50
	v_mul_f32_e32 v46, v42, v52
	v_fma_f32 v49, -v51, v46, v42
	v_fmac_f32_e32 v46, v49, v52
	v_fma_f32 v49, -v51, v46, v42
	v_lshlrev_b32_e32 v51, 16, v43
	v_mul_f32_e32 v42, 0xbfb8aa3b, v51
	v_mul_f32_e32 v43, 0xbfb8aa3b, v53
	v_exp_f32_e32 v42, v42
	v_exp_f32_e32 v43, v43
	v_div_fmas_f32 v46, v49, v52, v46
	v_div_fixup_f32 v46, v46, v48, v50
	v_pk_mul_f32 v[38:39], v[46:47], v[38:39]
	v_pk_add_f32 v[42:43], v[42:43], 1.0 op_sel_hi:[1,0]
	v_cvt_pk_bf16_f32 v38, v38, v39
	v_div_scale_f32 v46, s[2:3], v43, v43, v53
	v_rcp_f32_e32 v47, v46
	v_pk_mul_f32 v[34:35], v[34:35], v[14:15] op_sel_hi:[1,0]
	v_pk_mul_f32 v[32:33], v[32:33], v[14:15] op_sel_hi:[1,0]
	v_pk_mul_f32 v[30:31], v[30:31], v[14:15] op_sel_hi:[1,0]
	v_fma_f32 v39, -v46, v47, 1.0
	v_fmac_f32_e32 v47, v39, v47
	v_div_scale_f32 v39, vcc, v53, v43, v53
	v_mul_f32_e32 v40, v39, v47
	v_fma_f32 v41, -v46, v40, v39
	v_fmac_f32_e32 v40, v41, v47
	v_fma_f32 v39, -v46, v40, v39
	v_div_scale_f32 v46, s[2:3], v42, v42, v51
	v_rcp_f32_e32 v48, v46
	v_div_fmas_f32 v39, v39, v47, v40
	v_div_fixup_f32 v41, v39, v43, v53
	v_pk_mul_f32 v[28:29], v[28:29], v[14:15] op_sel_hi:[1,0]
	v_fma_f32 v39, -v46, v48, 1.0
	v_fmac_f32_e32 v48, v39, v48
	v_div_scale_f32 v39, vcc, v51, v42, v51
	v_mul_f32_e32 v40, v39, v48
	v_fma_f32 v43, -v46, v40, v39
	v_fmac_f32_e32 v40, v43, v48
	v_fma_f32 v39, -v46, v40, v39
	v_div_fmas_f32 v39, v39, v48, v40
	v_div_fixup_f32 v40, v39, v42, v51
	v_pk_mul_f32 v[36:37], v[40:41], v[36:37]
	v_lshlrev_b32_e32 v46, 16, v44
	v_cvt_pk_bf16_f32 v39, v36, v37
	global_store_dwordx2 v[8:9], v[38:39], off
	s_waitcnt vmcnt(3)
	s_nop 1
	v_mov_b32_e32 v36, v240
	v_mov_b32_e32 v37, v241
	v_mov_b32_e32 v38, v242
	v_mov_b32_e32 v39, v243
	global_load_dwordx4 v[240:243], v[12:13], off offset:256
	v_and_b32_e32 v42, 0xffff0000, v44
	v_mul_f32_e32 v40, 0xbfb8aa3b, v46
	v_mul_f32_e32 v41, 0xbfb8aa3b, v42
	v_exp_f32_e32 v40, v40
	v_exp_f32_e32 v41, v41
	v_pk_mul_f32 v[26:27], v[26:27], v[14:15] op_sel_hi:[1,0]
	v_pk_mul_f32 v[24:25], v[24:25], v[14:15] op_sel_hi:[1,0]
	v_pk_mul_f32 v[22:23], v[22:23], v[14:15] op_sel_hi:[1,0]
	v_pk_add_f32 v[40:41], v[40:41], 1.0 op_sel_hi:[1,0]
	v_pk_mul_f32 v[20:21], v[20:21], v[14:15] op_sel_hi:[1,0]
	v_div_scale_f32 v43, s[2:3], v41, v41, v42
	v_rcp_f32_e32 v44, v43
	v_pk_mul_f32 v[18:19], v[18:19], v[14:15] op_sel_hi:[1,0]
	v_pk_mul_f32 v[16:17], v[16:17], v[14:15] op_sel_hi:[1,0]
	v_pk_mul_f32 v[34:35], v[36:37], v[34:35]
	v_fma_f32 v36, -v43, v44, 1.0
	v_fmac_f32_e32 v44, v36, v44
	v_div_scale_f32 v36, vcc, v42, v41, v42
	v_mul_f32_e32 v37, v36, v44
	v_fma_f32 v47, -v43, v37, v36
	v_fmac_f32_e32 v37, v47, v44
	v_fma_f32 v36, -v43, v37, v36
	v_div_scale_f32 v43, s[2:3], v40, v40, v46
	v_rcp_f32_e32 v47, v43
	v_div_fmas_f32 v36, v36, v44, v37
	v_div_fixup_f32 v37, v36, v41, v42
	v_lshlrev_b32_e32 v44, 16, v45
	v_fma_f32 v36, -v43, v47, 1.0
	v_fmac_f32_e32 v47, v36, v47
	v_div_scale_f32 v36, vcc, v46, v40, v46
	v_mul_f32_e32 v41, v36, v47
	v_fma_f32 v42, -v43, v41, v36
	v_fmac_f32_e32 v41, v42, v47
	v_and_b32_e32 v45, 0xffff0000, v45
	v_fma_f32 v36, -v43, v41, v36
	v_mul_f32_e32 v42, 0xbfb8aa3b, v44
	v_mul_f32_e32 v43, 0xbfb8aa3b, v45
	v_exp_f32_e32 v42, v42
	v_exp_f32_e32 v43, v43
	v_div_fmas_f32 v36, v36, v47, v41
	v_div_fixup_f32 v36, v36, v40, v46
	v_pk_mul_f32 v[34:35], v[36:37], v[34:35]
	v_pk_add_f32 v[36:37], v[42:43], 1.0 op_sel_hi:[1,0]
	v_cvt_pk_bf16_f32 v34, v34, v35
	v_div_scale_f32 v40, s[2:3], v37, v37, v45
	v_rcp_f32_e32 v41, v40
	v_pk_mul_f32 v[32:33], v[38:39], v[32:33]
	v_fma_f32 v35, -v40, v41, 1.0
	v_fmac_f32_e32 v41, v35, v41
	v_div_scale_f32 v35, vcc, v45, v37, v45
	v_mul_f32_e32 v38, v35, v41
	v_fma_f32 v39, -v40, v38, v35
	v_fmac_f32_e32 v38, v39, v41
	v_div_scale_f32 v39, s[2:3], v36, v36, v44
	v_fma_f32 v35, -v40, v38, v35
	v_rcp_f32_e32 v40, v39
	v_div_fmas_f32 v35, v35, v41, v38
	v_div_fixup_f32 v37, v35, v37, v45
	v_fma_f32 v35, -v39, v40, 1.0
	v_fmac_f32_e32 v40, v35, v40
	v_div_scale_f32 v35, vcc, v44, v36, v44
	v_mul_f32_e32 v38, v35, v40
	v_fma_f32 v41, -v39, v38, v35
	v_fmac_f32_e32 v38, v41, v40
	v_fma_f32 v35, -v39, v38, v35
	v_div_fmas_f32 v35, v35, v40, v38
	v_div_fixup_f32 v36, v35, v36, v44
	v_pk_mul_f32 v[32:33], v[36:37], v[32:33]
	ds_read2_b64 v[36:39], v15 offset0:8 offset1:12
	v_cvt_pk_bf16_f32 v35, v32, v33
	global_store_dwordx2 v[8:9], v[34:35], off offset:32
	s_waitcnt vmcnt(4)
	s_nop 1
	v_mov_b32_e32 v32, v244
	v_mov_b32_e32 v33, v245
	v_mov_b32_e32 v34, v246
	v_mov_b32_e32 v35, v247
	global_load_dwordx4 v[244:247], v[12:13], off offset:320
	s_waitcnt lgkmcnt(0)
; #define LAS __attribute__((address_space(3)))
; __device__ __forceinline__ float bflo(unsigned w) { return __uint_as_float(w << 16); }
; __device__ __forceinline__ float bfhi(unsigned w) { return __uint_as_float(w & 0xffff0000u); }
; __device__ __forceinline__ float silu_f(float x) { return x / (1.f + __expf(-x)); }
; __device__ __forceinline__ void retp_out_unit(int unit, const bf16_t* P, const float* rotg, const float* gamma_logit, const bf16_t* ST, const float* gain, bf16_t* AO, LAS unsigned char* lds) {
;     ...
;     const LAS unsigned char* gp = lds + RP_V1 + tl * R_RS + (4 * q) * 2; bf16_t* op = AO + (size_t)row * D + h * 128 + 4 * q; const float* gn = gain + h * 128 + 4 * q;
; #pragma unroll
;     for (int c = 0; c < 8; ++c) { const u32x2 gw = *(const LAS u32x2*)(gp + 32 * c); const f32x4 g4 = *(const f32x4*)(gn + 16 * c);
;         u32x2 o; o.x = pk2(acc[c][0] * rstd * g4[0] * silu_f(bflo(gw.x)), acc[c][1] * rstd * g4[1] * silu_f(bfhi(gw.x)));
;         o.y = pk2(acc[c][2] * rstd * g4[2] * silu_f(bflo(gw.y)), acc[c][3] * rstd * g4[3] * silu_f(bfhi(gw.y)));
;         *(u32x2*)(op + 16 * c) = o; }
	v_lshlrev_b32_e32 v42, 16, v36
	v_and_b32_e32 v36, 0xffff0000, v36
	v_mul_f32_e32 v40, 0xbfb8aa3b, v42
	v_mul_f32_e32 v41, 0xbfb8aa3b, v36
	v_exp_f32_e32 v40, v40
	v_exp_f32_e32 v41, v41
	v_pk_mul_f32 v[30:31], v[32:33], v[30:31]
	v_pk_add_f32 v[40:41], v[40:41], 1.0 op_sel_hi:[1,0]
	v_pk_mul_f32 v[28:29], v[34:35], v[28:29]
	v_div_scale_f32 v43, s[2:3], v41, v41, v36
	v_rcp_f32_e32 v44, v43
	s_nop 0
	v_fma_f32 v32, -v43, v44, 1.0
	v_fmac_f32_e32 v44, v32, v44
	v_div_scale_f32 v32, vcc, v36, v41, v36
	v_mul_f32_e32 v33, v32, v44
	v_fma_f32 v45, -v43, v33, v32
	v_fmac_f32_e32 v33, v45, v44
	v_fma_f32 v32, -v43, v33, v32
	v_div_scale_f32 v43, s[2:3], v40, v40, v42
	v_rcp_f32_e32 v45, v43
	v_div_fmas_f32 v32, v32, v44, v33
	v_div_fixup_f32 v33, v32, v41, v36
	v_and_b32_e32 v44, 0xffff0000, v37
	v_fma_f32 v32, -v43, v45, 1.0
	v_fmac_f32_e32 v45, v32, v45
	v_div_scale_f32 v32, vcc, v42, v40, v42
	v_mul_f32_e32 v41, v32, v45
	v_fma_f32 v36, -v43, v41, v32
	v_fmac_f32_e32 v41, v36, v45
	v_fma_f32 v32, -v43, v41, v32
	v_lshlrev_b32_e32 v43, 16, v37
	v_mul_f32_e32 v36, 0xbfb8aa3b, v43
	v_mul_f32_e32 v37, 0xbfb8aa3b, v44
	v_exp_f32_e32 v36, v36
	v_exp_f32_e32 v37, v37
	v_div_fmas_f32 v32, v32, v45, v41
	v_div_fixup_f32 v32, v32, v40, v42
	v_pk_mul_f32 v[30:31], v[32:33], v[30:31]
	v_pk_add_f32 v[32:33], v[36:37], 1.0 op_sel_hi:[1,0]
	v_cvt_pk_bf16_f32 v30, v30, v31
	v_div_scale_f32 v36, s[2:3], v33, v33, v44
	v_rcp_f32_e32 v37, v36
	s_nop 0
	v_fma_f32 v31, -v36, v37, 1.0
	v_fmac_f32_e32 v37, v31, v37
	v_div_scale_f32 v31, vcc, v44, v33, v44
	v_mul_f32_e32 v34, v31, v37
	v_fma_f32 v35, -v36, v34, v31
	v_fmac_f32_e32 v34, v35, v37
	v_div_scale_f32 v35, s[2:3], v32, v32, v43
	v_fma_f32 v31, -v36, v34, v31
	v_rcp_f32_e32 v36, v35
	v_div_fmas_f32 v31, v31, v37, v34
	v_div_fixup_f32 v33, v31, v33, v44
	v_fma_f32 v31, -v35, v36, 1.0
	v_fmac_f32_e32 v36, v31, v36
	v_div_scale_f32 v31, vcc, v43, v32, v43
	v_mul_f32_e32 v34, v31, v36
	v_fma_f32 v37, -v35, v34, v31
	v_fmac_f32_e32 v34, v37, v36
	v_fma_f32 v31, -v35, v34, v31
	v_div_fmas_f32 v31, v31, v36, v34
	v_div_fixup_f32 v32, v31, v32, v43
	v_pk_mul_f32 v[28:29], v[32:33], v[28:29]
	v_lshlrev_b32_e32 v36, 16, v38
	v_cvt_pk_bf16_f32 v31, v28, v29
	global_store_dwordx2 v[8:9], v[30:31], off offset:64
	s_waitcnt vmcnt(5)
	s_nop 1
	v_mov_b32_e32 v28, v248
	v_mov_b32_e32 v29, v249
	v_mov_b32_e32 v30, v250
	v_mov_b32_e32 v31, v251
	global_load_dwordx4 v[248:251], v[12:13], off offset:384
	v_and_b32_e32 v34, 0xffff0000, v38
	v_mul_f32_e32 v32, 0xbfb8aa3b, v36
	v_mul_f32_e32 v33, 0xbfb8aa3b, v34
	v_exp_f32_e32 v32, v32
	v_exp_f32_e32 v33, v33
	v_pk_mul_f32 v[26:27], v[28:29], v[26:27]
	v_pk_add_f32 v[32:33], v[32:33], 1.0 op_sel_hi:[1,0]
	v_pk_mul_f32 v[24:25], v[30:31], v[24:25]
	v_div_scale_f32 v35, s[2:3], v33, v33, v34
	v_rcp_f32_e32 v37, v35
	s_nop 0
	v_fma_f32 v28, -v35, v37, 1.0
	v_fmac_f32_e32 v37, v28, v37
	v_div_scale_f32 v28, vcc, v34, v33, v34
	v_mul_f32_e32 v29, v28, v37
	v_fma_f32 v38, -v35, v29, v28
	v_fmac_f32_e32 v29, v38, v37
	v_fma_f32 v28, -v35, v29, v28
	v_div_scale_f32 v35, s[2:3], v32, v32, v36
	v_rcp_f32_e32 v38, v35
	v_div_fmas_f32 v28, v28, v37, v29
	v_div_fixup_f32 v29, v28, v33, v34
	v_lshlrev_b32_e32 v37, 16, v39
	v_fma_f32 v28, -v35, v38, 1.0
	v_fmac_f32_e32 v38, v28, v38
	v_div_scale_f32 v28, vcc, v36, v32, v36
	v_mul_f32_e32 v33, v28, v38
	v_fma_f32 v34, -v35, v33, v28
	v_fmac_f32_e32 v33, v34, v38
	v_and_b32_e32 v39, 0xffff0000, v39
	v_fma_f32 v28, -v35, v33, v28
	v_mul_f32_e32 v34, 0xbfb8aa3b, v37
	v_mul_f32_e32 v35, 0xbfb8aa3b, v39
	v_exp_f32_e32 v34, v34
	v_exp_f32_e32 v35, v35
	v_div_fmas_f32 v28, v28, v38, v33
	v_div_fixup_f32 v28, v28, v32, v36
	v_pk_mul_f32 v[26:27], v[26:27], v[28:29]
	v_pk_add_f32 v[28:29], v[34:35], 1.0 op_sel_hi:[1,0]
	v_cvt_pk_bf16_f32 v26, v26, v27
	v_div_scale_f32 v32, s[2:3], v29, v29, v39
	v_rcp_f32_e32 v33, v32
	s_nop 0
	v_fma_f32 v27, -v32, v33, 1.0
	v_fmac_f32_e32 v33, v27, v33
	v_div_scale_f32 v27, vcc, v39, v29, v39
	v_mul_f32_e32 v30, v27, v33
	v_fma_f32 v31, -v32, v30, v27
	v_fmac_f32_e32 v30, v31, v33
	v_div_scale_f32 v31, s[2:3], v28, v28, v37
	v_fma_f32 v27, -v32, v30, v27
	v_rcp_f32_e32 v32, v31
	v_div_fmas_f32 v27, v27, v33, v30
	v_div_fixup_f32 v29, v27, v29, v39
	v_fma_f32 v27, -v31, v32, 1.0
	v_fmac_f32_e32 v32, v27, v32
	v_div_scale_f32 v27, vcc, v37, v28, v37
	v_mul_f32_e32 v30, v27, v32
	v_fma_f32 v33, -v31, v30, v27
	v_fmac_f32_e32 v30, v33, v32
	v_fma_f32 v27, -v31, v30, v27
	v_div_fmas_f32 v27, v27, v32, v30
	v_div_fixup_f32 v28, v27, v28, v37
	v_pk_mul_f32 v[24:25], v[24:25], v[28:29]
	ds_read2_b64 v[28:31], v15 offset0:16 offset1:20
	v_cvt_pk_bf16_f32 v27, v24, v25
	global_store_dwordx2 v[8:9], v[26:27], off offset:96
	s_waitcnt vmcnt(5)
	s_nop 1
	v_mov_b32_e32 v24, v240
	v_mov_b32_e32 v25, v241
	v_mov_b32_e32 v26, v242
	v_mov_b32_e32 v27, v243
	global_load_dwordx4 v[240:243], v[12:13], off offset:448
	s_waitcnt lgkmcnt(0)
; #define LAS __attribute__((address_space(3)))
; __device__ __forceinline__ float bflo(unsigned w) { return __uint_as_float(w << 16); }
; __device__ __forceinline__ float bfhi(unsigned w) { return __uint_as_float(w & 0xffff0000u); }
; __device__ __forceinline__ float silu_f(float x) { return x / (1.f + __expf(-x)); }
; __device__ __forceinline__ void retp_out_unit(int unit, const bf16_t* P, const float* rotg, const float* gamma_logit, const bf16_t* ST, const float* gain, bf16_t* AO, LAS unsigned char* lds) {
;     ...
;     const LAS unsigned char* gp = lds + RP_V1 + tl * R_RS + (4 * q) * 2; bf16_t* op = AO + (size_t)row * D + h * 128 + 4 * q; const float* gn = gain + h * 128 + 4 * q;
; #pragma unroll
;     for (int c = 0; c < 8; ++c) { const u32x2 gw = *(const LAS u32x2*)(gp + 32 * c); const f32x4 g4 = *(const f32x4*)(gn + 16 * c);
;         u32x2 o; o.x = pk2(acc[c][0] * rstd * g4[0] * silu_f(bflo(gw.x)), acc[c][1] * rstd * g4[1] * silu_f(bfhi(gw.x)));
;         o.y = pk2(acc[c][2] * rstd * g4[2] * silu_f(bflo(gw.y)), acc[c][3] * rstd * g4[3] * silu_f(bfhi(gw.y)));
;         *(u32x2*)(op + 16 * c) = o; }
	v_lshlrev_b32_e32 v34, 16, v28
	v_and_b32_e32 v28, 0xffff0000, v28
	v_mul_f32_e32 v32, 0xbfb8aa3b, v34
	v_mul_f32_e32 v33, 0xbfb8aa3b, v28
	v_exp_f32_e32 v32, v32
	v_exp_f32_e32 v33, v33
	v_pk_mul_f32 v[22:23], v[22:23], v[24:25]
	v_pk_add_f32 v[32:33], v[32:33], 1.0 op_sel_hi:[1,0]
	v_pk_mul_f32 v[20:21], v[20:21], v[26:27]
	v_div_scale_f32 v35, s[2:3], v33, v33, v28
	v_rcp_f32_e32 v36, v35
	s_nop 0
	v_fma_f32 v24, -v35, v36, 1.0
	v_fmac_f32_e32 v36, v24, v36
	v_div_scale_f32 v24, vcc, v28, v33, v28
	v_mul_f32_e32 v25, v24, v36
	v_fma_f32 v37, -v35, v25, v24
	v_fmac_f32_e32 v25, v37, v36
	v_fma_f32 v24, -v35, v25, v24
	v_div_scale_f32 v35, s[2:3], v32, v32, v34
	v_rcp_f32_e32 v37, v35
	v_div_fmas_f32 v24, v24, v36, v25
	v_div_fixup_f32 v25, v24, v33, v28
	v_and_b32_e32 v36, 0xffff0000, v29
	v_fma_f32 v24, -v35, v37, 1.0
	v_fmac_f32_e32 v37, v24, v37
	v_div_scale_f32 v24, vcc, v34, v32, v34
	v_mul_f32_e32 v33, v24, v37
	v_fma_f32 v28, -v35, v33, v24
	v_fmac_f32_e32 v33, v28, v37
	v_fma_f32 v24, -v35, v33, v24
	v_lshlrev_b32_e32 v35, 16, v29
	v_mul_f32_e32 v28, 0xbfb8aa3b, v35
	v_mul_f32_e32 v29, 0xbfb8aa3b, v36
	v_exp_f32_e32 v28, v28
	v_exp_f32_e32 v29, v29
	v_div_fmas_f32 v24, v24, v37, v33
	v_div_fixup_f32 v24, v24, v32, v34
	v_pk_mul_f32 v[22:23], v[22:23], v[24:25]
	v_pk_add_f32 v[24:25], v[28:29], 1.0 op_sel_hi:[1,0]
	v_cvt_pk_bf16_f32 v22, v22, v23
	v_div_scale_f32 v28, s[2:3], v25, v25, v36
	v_rcp_f32_e32 v29, v28
	s_nop 0
	v_fma_f32 v23, -v28, v29, 1.0
	v_fmac_f32_e32 v29, v23, v29
	v_div_scale_f32 v23, vcc, v36, v25, v36
	v_mul_f32_e32 v26, v23, v29
	v_fma_f32 v27, -v28, v26, v23
	v_fmac_f32_e32 v26, v27, v29
	v_div_scale_f32 v27, s[2:3], v24, v24, v35
	v_fma_f32 v23, -v28, v26, v23
	v_rcp_f32_e32 v28, v27
	v_div_fmas_f32 v23, v23, v29, v26
	v_div_fixup_f32 v25, v23, v25, v36
	v_fma_f32 v23, -v27, v28, 1.0
	v_fmac_f32_e32 v28, v23, v28
	v_div_scale_f32 v23, vcc, v35, v24, v35
	v_mul_f32_e32 v26, v23, v28
	v_fma_f32 v29, -v27, v26, v23
	v_fmac_f32_e32 v26, v29, v28
	v_fma_f32 v23, -v27, v26, v23
	v_div_fmas_f32 v23, v23, v28, v26
	v_div_fixup_f32 v24, v23, v24, v35
	v_pk_mul_f32 v[20:21], v[20:21], v[24:25]
	v_lshlrev_b32_e32 v28, 16, v30
	v_cvt_pk_bf16_f32 v23, v20, v21
	global_store_dwordx2 v[8:9], v[22:23], off offset:128
	s_waitcnt vmcnt(5)
	s_nop 1
	v_mov_b32_e32 v20, v244
	v_mov_b32_e32 v21, v245
	v_mov_b32_e32 v22, v246
	v_mov_b32_e32 v23, v247
	v_and_b32_e32 v26, 0xffff0000, v30
	v_mul_f32_e32 v24, 0xbfb8aa3b, v28
	v_mul_f32_e32 v25, 0xbfb8aa3b, v26
	v_exp_f32_e32 v24, v24
	v_exp_f32_e32 v25, v25
	v_pk_mul_f32 v[18:19], v[18:19], v[20:21]
	v_pk_add_f32 v[24:25], v[24:25], 1.0 op_sel_hi:[1,0]
	v_pk_mul_f32 v[16:17], v[16:17], v[22:23]
	v_div_scale_f32 v27, s[2:3], v25, v25, v26
	v_rcp_f32_e32 v29, v27
	s_nop 0
	v_fma_f32 v20, -v27, v29, 1.0
	v_fmac_f32_e32 v29, v20, v29
	v_div_scale_f32 v20, vcc, v26, v25, v26
	v_mul_f32_e32 v21, v20, v29
	v_fma_f32 v30, -v27, v21, v20
	v_fmac_f32_e32 v21, v30, v29
	v_fma_f32 v20, -v27, v21, v20
	v_div_scale_f32 v27, s[2:3], v24, v24, v28
	v_rcp_f32_e32 v30, v27
	v_div_fmas_f32 v20, v20, v29, v21
	v_div_fixup_f32 v21, v20, v25, v26
	v_lshlrev_b32_e32 v29, 16, v31
	v_fma_f32 v20, -v27, v30, 1.0
	v_fmac_f32_e32 v30, v20, v30
	v_div_scale_f32 v20, vcc, v28, v24, v28
	v_mul_f32_e32 v25, v20, v30
	v_fma_f32 v26, -v27, v25, v20
	v_fmac_f32_e32 v25, v26, v30
	v_and_b32_e32 v31, 0xffff0000, v31
	v_fma_f32 v20, -v27, v25, v20
	v_mul_f32_e32 v26, 0xbfb8aa3b, v29
	v_mul_f32_e32 v27, 0xbfb8aa3b, v31
	v_exp_f32_e32 v26, v26
	v_exp_f32_e32 v27, v27
	v_div_fmas_f32 v20, v20, v30, v25
	v_div_fixup_f32 v20, v20, v24, v28
	v_pk_mul_f32 v[18:19], v[18:19], v[20:21]
	v_pk_add_f32 v[20:21], v[26:27], 1.0 op_sel_hi:[1,0]
	v_cvt_pk_bf16_f32 v18, v18, v19
	v_div_scale_f32 v24, s[2:3], v21, v21, v31
	v_rcp_f32_e32 v25, v24
	s_nop 0
	v_fma_f32 v19, -v24, v25, 1.0
	v_fmac_f32_e32 v25, v19, v25
	v_div_scale_f32 v19, vcc, v31, v21, v31
	v_mul_f32_e32 v22, v19, v25
	v_fma_f32 v23, -v24, v22, v19
	v_fmac_f32_e32 v22, v23, v25
	v_div_scale_f32 v23, s[2:3], v20, v20, v29
	v_fma_f32 v19, -v24, v22, v19
	v_rcp_f32_e32 v24, v23
	v_div_fmas_f32 v19, v19, v25, v22
	v_div_fixup_f32 v21, v19, v21, v31
	v_fma_f32 v19, -v23, v24, 1.0
	v_fmac_f32_e32 v24, v19, v24
	v_div_scale_f32 v19, vcc, v29, v20, v29
	v_mul_f32_e32 v22, v19, v24
	v_fma_f32 v25, -v23, v22, v19
	v_fmac_f32_e32 v22, v25, v24
	v_fma_f32 v19, -v23, v22, v19
	v_div_fmas_f32 v19, v19, v24, v22
	v_div_fixup_f32 v20, v19, v20, v29
	v_pk_mul_f32 v[16:17], v[16:17], v[20:21]
	ds_read2_b64 v[20:23], v15 offset0:24 offset1:28
	v_cvt_pk_bf16_f32 v19, v16, v17
	global_store_dwordx2 v[8:9], v[18:19], off offset:160
	s_waitcnt vmcnt(4)
	s_nop 1
	v_mov_b32_e32 v16, v248
	v_mov_b32_e32 v17, v249
	v_mov_b32_e32 v18, v250
	v_mov_b32_e32 v19, v251
	s_waitcnt lgkmcnt(0)
; #define LAS __attribute__((address_space(3)))
; __device__ __forceinline__ float bflo(unsigned w) { return __uint_as_float(w << 16); }
; __device__ __forceinline__ float bfhi(unsigned w) { return __uint_as_float(w & 0xffff0000u); }
; __device__ __forceinline__ float silu_f(float x) { return x / (1.f + __expf(-x)); }
; __device__ __forceinline__ void retp_out_unit(int unit, const bf16_t* P, const float* rotg, const float* gamma_logit, const bf16_t* ST, const float* gain, bf16_t* AO, LAS unsigned char* lds) {
;     ...
;     const LAS unsigned char* gp = lds + RP_V1 + tl * R_RS + (4 * q) * 2; bf16_t* op = AO + (size_t)row * D + h * 128 + 4 * q; const float* gn = gain + h * 128 + 4 * q;
; #pragma unroll
;     for (int c = 0; c < 8; ++c) { const u32x2 gw = *(const LAS u32x2*)(gp + 32 * c); const f32x4 g4 = *(const f32x4*)(gn + 16 * c);
;         u32x2 o; o.x = pk2(acc[c][0] * rstd * g4[0] * silu_f(bflo(gw.x)), acc[c][1] * rstd * g4[1] * silu_f(bfhi(gw.x)));
;         o.y = pk2(acc[c][2] * rstd * g4[2] * silu_f(bflo(gw.y)), acc[c][3] * rstd * g4[3] * silu_f(bfhi(gw.y)));
;         *(u32x2*)(op + 16 * c) = o; }
	v_lshlrev_b32_e32 v15, 16, v20
	v_and_b32_e32 v20, 0xffff0000, v20
	v_mul_f32_e32 v24, 0xbfb8aa3b, v15
	v_mul_f32_e32 v25, 0xbfb8aa3b, v20
	v_exp_f32_e32 v24, v24
	v_exp_f32_e32 v25, v25
	v_pk_mul_f32 v[10:11], v[10:11], v[14:15] op_sel_hi:[1,0]
	v_pk_add_f32 v[24:25], v[24:25], 1.0 op_sel_hi:[1,0]
	s_nop 0
	v_div_scale_f32 v26, s[2:3], v25, v25, v20
	v_rcp_f32_e32 v27, v26
	v_pk_mul_f32 v[10:11], v[10:11], v[16:17]
	v_fma_f32 v16, -v26, v27, 1.0
	v_fmac_f32_e32 v27, v16, v27
	v_div_scale_f32 v16, vcc, v20, v25, v20
	v_mul_f32_e32 v17, v16, v27
	v_fma_f32 v28, -v26, v17, v16
	v_fmac_f32_e32 v17, v28, v27
	v_fma_f32 v16, -v26, v17, v16
	v_div_scale_f32 v26, s[2:3], v24, v24, v15
	v_rcp_f32_e32 v28, v26
	v_div_fmas_f32 v16, v16, v27, v17
	v_div_fixup_f32 v17, v16, v25, v20
	v_and_b32_e32 v27, 0xffff0000, v21
	v_fma_f32 v16, -v26, v28, 1.0
	v_fmac_f32_e32 v28, v16, v28
	v_div_scale_f32 v16, vcc, v15, v24, v15
	v_mul_f32_e32 v25, v16, v28
	v_fma_f32 v20, -v26, v25, v16
	v_fmac_f32_e32 v25, v20, v28
	v_fma_f32 v16, -v26, v25, v16
	v_lshlrev_b32_e32 v26, 16, v21
	v_mul_f32_e32 v20, 0xbfb8aa3b, v26
	v_mul_f32_e32 v21, 0xbfb8aa3b, v27
	v_exp_f32_e32 v20, v20
	v_exp_f32_e32 v21, v21
	v_div_fmas_f32 v16, v16, v28, v25
	v_div_fixup_f32 v16, v16, v24, v15
	v_pk_mul_f32 v[10:11], v[10:11], v[16:17]
	v_pk_add_f32 v[16:17], v[20:21], 1.0 op_sel_hi:[1,0]
	v_cvt_pk_bf16_f32 v10, v10, v11
	v_div_scale_f32 v15, s[2:3], v17, v17, v27
	v_rcp_f32_e32 v20, v15
	v_pk_mul_f32 v[6:7], v[6:7], v[14:15] op_sel_hi:[1,0]
	v_fma_f32 v11, -v15, v20, 1.0
	v_fmac_f32_e32 v20, v11, v20
	v_div_scale_f32 v11, vcc, v27, v17, v27
	v_pk_mul_f32 v[6:7], v[6:7], v[18:19]
	v_mul_f32_e32 v18, v11, v20
	v_fma_f32 v19, -v15, v18, v11
	v_fmac_f32_e32 v18, v19, v20
	v_fma_f32 v11, -v15, v18, v11
	v_div_scale_f32 v15, s[2:3], v16, v16, v26
	v_rcp_f32_e32 v19, v15
	v_div_fmas_f32 v11, v11, v20, v18
	v_div_fixup_f32 v17, v11, v17, v27
	v_fma_f32 v11, -v15, v19, 1.0
	v_fmac_f32_e32 v19, v11, v19
	v_div_scale_f32 v11, vcc, v26, v16, v26
	v_mul_f32_e32 v18, v11, v19
	v_fma_f32 v20, -v15, v18, v11
	v_fmac_f32_e32 v18, v20, v19
	v_fma_f32 v11, -v15, v18, v11
	v_div_fmas_f32 v11, v11, v19, v18
	v_div_fixup_f32 v16, v11, v16, v26
	v_pk_mul_f32 v[6:7], v[6:7], v[16:17]
	v_lshlrev_b32_e32 v15, 16, v22
	v_cvt_pk_bf16_f32 v11, v6, v7
	global_store_dwordx2 v[8:9], v[10:11], off offset:192
	s_waitcnt vmcnt(3)
	s_nop 1
	v_mov_b32_e32 v10, v240
	v_mov_b32_e32 v11, v241
	v_mov_b32_e32 v12, v242
	v_mov_b32_e32 v13, v243
	v_and_b32_e32 v16, 0xffff0000, v22
	v_mul_f32_e32 v6, 0xbfb8aa3b, v15
	v_mul_f32_e32 v7, 0xbfb8aa3b, v16
	v_exp_f32_e32 v6, v6
	v_exp_f32_e32 v7, v7
	v_pk_mul_f32 v[4:5], v[4:5], v[14:15] op_sel_hi:[1,0]
	v_and_b32_e32 v20, 0xffff0000, v23
	v_pk_mul_f32 v[2:3], v[2:3], v[14:15] op_sel_hi:[1,0]
	v_pk_add_f32 v[6:7], v[6:7], 1.0 op_sel_hi:[1,0]
	v_pk_mul_f32 v[4:5], v[4:5], v[10:11]
	v_div_scale_f32 v17, s[2:3], v7, v7, v16
	v_rcp_f32_e32 v18, v17
	v_pk_mul_f32 v[2:3], v[2:3], v[12:13]
	v_fma_f32 v10, -v17, v18, 1.0
	v_fmac_f32_e32 v18, v10, v18
	v_div_scale_f32 v10, vcc, v16, v7, v16
	v_mul_f32_e32 v11, v10, v18
	v_fma_f32 v19, -v17, v11, v10
	v_fmac_f32_e32 v11, v19, v18
	v_fma_f32 v10, -v17, v11, v10
	v_div_scale_f32 v17, s[2:3], v6, v6, v15
	v_rcp_f32_e32 v19, v17
	v_div_fmas_f32 v10, v10, v18, v11
	v_div_fixup_f32 v7, v10, v7, v16
	v_lshlrev_b32_e32 v18, 16, v23
	v_fma_f32 v10, -v17, v19, 1.0
	v_fmac_f32_e32 v19, v10, v19
	v_div_scale_f32 v10, vcc, v15, v6, v15
	v_mul_f32_e32 v16, v10, v19
	v_fma_f32 v11, -v17, v16, v10
	v_fmac_f32_e32 v16, v11, v19
	v_fma_f32 v17, -v17, v16, v10
	v_mul_f32_e32 v10, 0xbfb8aa3b, v18
	v_mul_f32_e32 v11, 0xbfb8aa3b, v20
	v_exp_f32_e32 v10, v10
	v_exp_f32_e32 v11, v11
	v_div_fmas_f32 v16, v17, v19, v16
	v_div_fixup_f32 v6, v16, v6, v15
	v_pk_mul_f32 v[4:5], v[4:5], v[6:7]
	v_pk_add_f32 v[6:7], v[10:11], 1.0 op_sel_hi:[1,0]
	v_cvt_pk_bf16_f32 v4, v4, v5
	v_div_scale_f32 v10, s[2:3], v7, v7, v20
	v_rcp_f32_e32 v11, v10
	s_nop 0
	v_fma_f32 v5, -v10, v11, 1.0
	v_fmac_f32_e32 v11, v5, v11
	v_div_scale_f32 v5, vcc, v20, v7, v20
	v_mul_f32_e32 v12, v5, v11
	v_fma_f32 v13, -v10, v12, v5
	v_fmac_f32_e32 v12, v13, v11
	v_fma_f32 v5, -v10, v12, v5
	v_div_scale_f32 v10, s[2:3], v6, v6, v18
	v_rcp_f32_e32 v13, v10
	v_div_fmas_f32 v5, v5, v11, v12
	v_div_fixup_f32 v7, v5, v7, v20
	v_fma_f32 v5, -v10, v13, 1.0
	v_fmac_f32_e32 v13, v5, v13
	v_div_scale_f32 v5, vcc, v18, v6, v18
	v_mul_f32_e32 v11, v5, v13
	v_fma_f32 v12, -v10, v11, v5
	v_fmac_f32_e32 v11, v12, v13
	v_fma_f32 v5, -v10, v11, v5
	v_div_fmas_f32 v5, v5, v13, v11
	v_div_fixup_f32 v6, v5, v6, v18
	v_pk_mul_f32 v[2:3], v[2:3], v[6:7]
	s_nop 0
	v_cvt_pk_bf16_f32 v5, v2, v3
	global_store_dwordx2 v[8:9], v[4:5], off offset:224
	s_cbranch_scc0 .LBB0_472
